# baseline (speedup 1.0000x reference)
.Lmk_nomax:
	v_sub_f32_e32 v34, v34, v195
	v_fmamk_f32 v34, v34, 0x3fb8aa3b, v187
	v_exp_f32_e32 v34, v34
	s_nop 0
	v_cvt_f16_f32_e32 v34, v34
	v_cndmask_b32_e64 v34, 0, v34, s[56:57]
	ds_write_b16 v115, v34
	ds_read_b64_tr_b16 v[200:201], v193 offset:0
	ds_read_b64_tr_b16 v[202:203], v193 offset:512
	ds_read_b64_tr_b16 v[160:161], v193 offset:1024
	ds_read_b64_tr_b16 v[162:163], v193 offset:1536
	s_and_b64 vcc, exec, s[54:55]
	s_cbranch_vccnz .Lmk_first_path
	s_waitcnt vmcnt(0)
	s_waitcnt lgkmcnt(0)
	v_mfma_f32_16x16x32_f16 v[54:57], v[130:133], v[200:203], v[54:57]
	ds_write_b128 v196, v[10:13]
	v_mfma_f32_16x16x32_f16 v[58:61], v[134:137], v[200:203], v[58:61]
	ds_write_b128 v196, v[14:17] offset:1024
	v_mfma_f32_16x16x32_f16 v[62:65], v[138:141], v[200:203], v[62:65]
	ds_write_b128 v196, v[30:33] offset:2048
	v_mfma_f32_16x16x32_f16 v[66:69], v[142:145], v[200:203], v[66:69]
	ds_write_b128 v196, v[26:29] offset:3072
	v_mfma_f32_16x16x32_f16 v[70:73], v[168:171], v[200:203], v[70:73]
	ds_write_b16 v115, v35
